# rwkv_pre S0: per-wave segment prefix reads all seven partial sums at once (same summation order) instead of a serial LDS read loop
# baseline (speedup 1.0000x reference)
.LBB0_603:
	v_add_f32_e32 v211, 0, v240
	v_add_f32_e32 v210, v211, v241
	v_add_f32_e32 v219, v210, v242
	v_add_f32_e32 v209, v219, v243
	v_add_f32_e32 v243, v209, v244
	v_add_f32_e32 v242, v243, v245
	v_ashrrev_i32_e32 v248, 6, v0
	v_add_f32_e32 v241, v242, v246
	v_lshl_add_u32 v182, v0, 2, 0
	v_and_b32_e32 v249, 63, v0
	v_mov_b32_e32 v250, 0
	v_add_f32_e32 v240, v241, v247
	v_add_u32_e32 v182, 0x27400, v182
	v_cmp_lt_i32_e32 vcc, 0, v248
	ds_write_b32 v182, v240
	s_waitcnt lgkmcnt(0)
	s_barrier
	s_and_saveexec_b64 s[0:1], vcc
	s_cbranch_execz .LBB0_607
	s_add_i32 s2, 0, 0x27400
	v_lshl_add_u32 v244, v249, 2, s2
	ds_read_b32 v2, v244
	ds_read_b32 v3, v244 offset:256
	ds_read_b32 v4, v244 offset:512
	ds_read_b32 v5, v244 offset:768
	ds_read_b32 v6, v244 offset:1024
	ds_read_b32 v7, v244 offset:1280
	ds_read_b32 v8, v244 offset:1536
	v_readfirstlane_b32 s2, v248
	v_mov_b32_e32 v250, 0
	s_waitcnt lgkmcnt(0)
	v_add_f32_e32 v250, v250, v2
	s_cmp_gt_u32 s2, 1
	s_cbranch_scc0 .Lsegs_done
	v_add_f32_e32 v250, v250, v3
	s_cmp_gt_u32 s2, 2
	s_cbranch_scc0 .Lsegs_done
	v_add_f32_e32 v250, v250, v4
	s_cmp_gt_u32 s2, 3
	s_cbranch_scc0 .Lsegs_done
	v_add_f32_e32 v250, v250, v5
	s_cmp_gt_u32 s2, 4
	s_cbranch_scc0 .Lsegs_done
	v_add_f32_e32 v250, v250, v6
	s_cmp_gt_u32 s2, 5
	s_cbranch_scc0 .Lsegs_done
	v_add_f32_e32 v250, v250, v7
	s_cmp_gt_u32 s2, 6
	s_cbranch_scc0 .Lsegs_done
	v_add_f32_e32 v250, v250, v8
.Lsegs_done:
.LBB0_607:
	s_or_b64 exec, exec, s[0:1]
	s_add_i32 s0, s10, 0x5ff
	s_cmpk_lt_u32 s0, 0xbff
	v_lshrrev_b32_e32 v182, 16, v25
	s_cselect_b64 vcc, -1, 0
	v_cndmask_b32_e32 v25, v182, v25, vcc
	v_lshrrev_b32_e32 v182, 16, v20
	v_cndmask_b32_e32 v182, v182, v20, vcc
	v_lshrrev_b32_e32 v20, 16, v21
	v_cndmask_b32_e32 v183, v20, v21, vcc
	v_lshrrev_b32_e32 v20, 16, v32
	v_cndmask_b32_e32 v32, v20, v32, vcc
	v_lshrrev_b32_e32 v20, 16, v33
	v_cndmask_b32_e32 v33, v20, v33, vcc
	v_lshrrev_b32_e32 v20, 16, v28
	v_cndmask_b32_e32 v28, v20, v28, vcc
	v_lshrrev_b32_e32 v20, 16, v29
	v_cndmask_b32_e32 v29, v20, v29, vcc
	v_lshrrev_b32_e32 v20, 16, v176
	v_cndmask_b32_e32 v176, v20, v176, vcc
	v_lshrrev_b32_e32 v20, 16, v177
	v_cndmask_b32_e32 v177, v20, v177, vcc
	v_lshrrev_b32_e32 v20, 16, v168
	v_cndmask_b32_e32 v168, v20, v168, vcc
	v_lshrrev_b32_e32 v20, 16, v169
	v_cndmask_b32_e32 v169, v20, v169, vcc
	v_lshrrev_b32_e32 v20, 16, v180
	v_cndmask_b32_e32 v180, v20, v180, vcc
	v_lshrrev_b32_e32 v20, 16, v181
	v_cndmask_b32_e32 v181, v20, v181, vcc
	v_lshrrev_b32_e32 v20, 16, v172
	v_cndmask_b32_e32 v184, v20, v172, vcc
	v_lshrrev_b32_e32 v20, 16, v173
	v_cndmask_b32_e32 v173, v20, v173, vcc
	v_add_f32_e32 v20, v211, v250
	v_mul_f32_e32 v21, 0x3fb8aa3b, v250
	v_exp_f32_e32 v21, v21
	v_mul_f32_e32 v172, 0xbfb8aa3b, v20
	v_exp_f32_e32 v172, v172
	v_mul_f32_e32 v20, 0x3fb8aa3b, v20
	v_exp_f32_e32 v185, v20
	v_lshlrev_b32_e32 v20, 16, v23
	v_cndmask_b32_sdwa v24, v24, v24, vcc dst_sel:WORD_1 dst_unused:UNUSED_PAD src0_sel:WORD_1 src1_sel:DWORD
	v_mul_f32_e64 v20, v21, -v20
	v_cvt_pk_bf16_f32 v23, v20, s0
	v_mul_f32_e32 v20, v172, v24
	v_cvt_pk_bf16_f32 v21, v20, s0
	v_lshlrev_b32_e32 v20, 16, v25
	v_lshlrev_b32_e32 v24, 16, v22
	v_mul_f32_e32 v20, v172, v20
	v_mul_f32_e32 v24, v185, v24
	v_cvt_pk_bf16_f32 v20, v20, s0
	v_cvt_pk_bf16_f32 v24, v24, s0
	s_movk_i32 s0, 0x240
	v_mul_lo_u32 v25, v248, s0
	v_or_b32_e32 v25, v25, v249
	v_lshl_add_u32 v211, v25, 1, 0
	ds_write_b16 v211, v23
	ds_write_b16 v211, v21 offset:9216
	ds_write_b16 v211, v20 offset:18432
	ds_write_b16 v211, v24 offset:27648
	v_add_f32_e32 v23, v210, v250
	v_mul_f32_e32 v24, 0xbfb8aa3b, v23
	v_exp_f32_e32 v24, v24
	v_lshlrev_b32_e32 v19, 16, v19
	v_mul_f32_e32 v23, 0x3fb8aa3b, v23
	v_mul_f32_e64 v19, v185, -v19
	v_exp_f32_e32 v25, v23
	v_cvt_pk_bf16_f32 v172, v19, s0
	v_lshlrev_b32_e32 v19, 16, v182
	v_mul_f32_e32 v19, v24, v19
	v_cvt_pk_bf16_f32 v23, v19, s0
	v_lshlrev_b32_e32 v19, 16, v183
	v_mul_f32_e32 v19, v24, v19
	v_lshlrev_b32_e32 v24, 16, v18
	v_mul_f32_e32 v24, v25, v24
	v_cvt_pk_bf16_f32 v24, v24, s0
	v_cvt_pk_bf16_f32 v19, v19, s0
	ds_write_b16 v211, v172 offset:144
	ds_write_b16 v211, v23 offset:9360
	ds_write_b16 v211, v19 offset:18576
	ds_write_b16 v211, v24 offset:27792
	v_add_f32_e32 v24, v219, v250
	v_mul_f32_e32 v172, 0xbfb8aa3b, v24
	v_exp_f32_e32 v172, v172
	v_mul_f32_e32 v24, 0x3fb8aa3b, v24
	v_exp_f32_e32 v182, v24
	v_lshlrev_b32_e32 v24, 16, v31
	v_mul_f32_e64 v24, v25, -v24
	v_cvt_pk_bf16_f32 v31, v24, s0
	v_lshlrev_b32_e32 v24, 16, v32
	v_mul_f32_e32 v24, v172, v24
	v_cvt_pk_bf16_f32 v25, v24, s0
	v_lshlrev_b32_e32 v24, 16, v33
	v_lshlrev_b32_e32 v32, 16, v30
	v_mul_f32_e32 v24, v172, v24
	v_mul_f32_e32 v32, v182, v32
	v_cvt_pk_bf16_f32 v24, v24, s0
	v_cvt_pk_bf16_f32 v32, v32, s0
	ds_write_b16 v211, v31 offset:288
	ds_write_b16 v211, v25 offset:9504
	ds_write_b16 v211, v24 offset:18720
	ds_write_b16 v211, v32 offset:27936
	v_add_f32_e32 v31, v209, v250
	v_mul_f32_e32 v32, 0xbfb8aa3b, v31
	v_exp_f32_e32 v32, v32
	v_mul_f32_e32 v31, 0x3fb8aa3b, v31
	v_lshlrev_b32_e32 v27, 16, v27
	v_exp_f32_e32 v31, v31
	v_mul_f32_e64 v27, v182, -v27
	v_cvt_pk_bf16_f32 v33, v27, s0
	v_lshlrev_b32_e32 v27, 16, v28
	v_mul_f32_e32 v27, v32, v27
	v_cvt_pk_bf16_f32 v28, v27, s0
	v_lshlrev_b32_e32 v27, 16, v29
	v_lshlrev_b32_e32 v29, 16, v26
	v_mul_f32_e32 v29, v31, v29
	v_mul_f32_e32 v27, v32, v27
	v_cvt_pk_bf16_f32 v29, v29, s0
	v_cvt_pk_bf16_f32 v27, v27, s0
	ds_write_b16 v211, v33 offset:432
	ds_write_b16 v211, v28 offset:9648
	ds_write_b16 v211, v27 offset:18864
	ds_write_b16 v211, v29 offset:28080
	v_add_f32_e32 v29, v243, v250
	v_mul_f32_e32 v32, 0xbfb8aa3b, v29
	v_exp_f32_e32 v32, v32
	v_mul_f32_e32 v29, 0x3fb8aa3b, v29
	v_exp_f32_e32 v33, v29
	v_lshlrev_b32_e32 v29, 16, v175
	v_mul_f32_e64 v29, v31, -v29
	v_cvt_pk_bf16_f32 v172, v29, s0
	v_lshlrev_b32_e32 v29, 16, v176
	v_mul_f32_e32 v29, v32, v29
	v_cvt_pk_bf16_f32 v31, v29, s0
	v_lshlrev_b32_e32 v29, 16, v177
	v_mul_f32_e32 v29, v32, v29
	v_lshlrev_b32_e32 v32, 16, v174
	v_mul_f32_e32 v32, v33, v32
	v_cvt_pk_bf16_f32 v32, v32, s0
	v_cvt_pk_bf16_f32 v29, v29, s0
	ds_write_b16 v211, v172 offset:576
	ds_write_b16 v211, v31 offset:9792
	ds_write_b16 v211, v29 offset:19008
	ds_write_b16 v211, v32 offset:28224
	v_add_f32_e32 v32, v242, v250
	v_mul_f32_e32 v172, 0xbfb8aa3b, v32
	v_exp_f32_e32 v172, v172
	v_mul_f32_e32 v32, 0x3fb8aa3b, v32
	v_exp_f32_e32 v175, v32
	v_lshlrev_b32_e32 v32, 16, v167
	v_mul_f32_e64 v32, v33, -v32
	v_cvt_pk_bf16_f32 v167, v32, s0
	v_lshlrev_b32_e32 v32, 16, v168
	v_mul_f32_e32 v32, v172, v32
	v_cvt_pk_bf16_f32 v33, v32, s0
	v_lshlrev_b32_e32 v32, 16, v169
	v_lshlrev_b32_e32 v168, 16, v166
	v_mul_f32_e32 v32, v172, v32
	v_mul_f32_e32 v168, v175, v168
	v_cvt_pk_bf16_f32 v32, v32, s0
	v_cvt_pk_bf16_f32 v168, v168, s0
	ds_write_b16 v211, v167 offset:720
	ds_write_b16 v211, v33 offset:9936
	ds_write_b16 v211, v32 offset:19152
	ds_write_b16 v211, v168 offset:28368
	v_add_f32_e32 v167, v241, v250
	v_mul_f32_e32 v168, 0xbfb8aa3b, v167
	v_exp_f32_e32 v169, v168
	v_mul_f32_e32 v167, 0x3fb8aa3b, v167
	v_exp_f32_e32 v176, v167
	v_lshlrev_b32_e32 v167, 16, v179
	v_mul_f32_e64 v167, v175, -v167
	v_cvt_pk_bf16_f32 v172, v167, s0
	v_lshlrev_b32_e32 v167, 16, v180
	v_mul_f32_e32 v167, v169, v167
	v_cvt_pk_bf16_f32 v168, v167, s0
	v_lshlrev_b32_e32 v167, 16, v181
	v_mul_f32_e32 v167, v169, v167
	v_lshlrev_b32_e32 v169, 16, v178
	v_mul_f32_e32 v169, v176, v169
	v_cvt_pk_bf16_f32 v169, v169, s0
	v_cvt_pk_bf16_f32 v167, v167, s0
	ds_write_b16 v211, v172 offset:864
	ds_write_b16 v211, v168 offset:10080
	ds_write_b16 v211, v167 offset:19296
	ds_write_b16 v211, v169 offset:28512
	v_add_f32_e32 v169, v240, v250
	v_mul_f32_e32 v172, 0xbfb8aa3b, v169
	v_exp_f32_e32 v175, v172
	v_mul_f32_e32 v169, 0x3fb8aa3b, v169
	v_exp_f32_e32 v172, v169
	v_lshlrev_b32_e32 v169, 16, v171
	v_mul_f32_e64 v169, v176, -v169
	v_cvt_pk_bf16_f32 v176, v169, s0
	v_lshlrev_b32_e32 v169, 16, v184
	v_mul_f32_e32 v169, v175, v169
	v_cvt_pk_bf16_f32 v171, v169, s0
	v_lshlrev_b32_e32 v169, 16, v173
	v_mul_f32_e32 v169, v175, v169
	v_lshlrev_b32_e32 v173, 16, v170
	v_cvt_pk_bf16_f32 v169, v169, s0
	v_mul_f32_e32 v173, v172, v173
	v_cmp_eq_u32_e32 vcc, 7, v248
	v_cvt_pk_bf16_f32 v173, v173, s0
	ds_write_b16 v211, v176 offset:1008
	ds_write_b16 v211, v171 offset:10224
	ds_write_b16 v211, v169 offset:19440
	ds_write_b16 v211, v173 offset:28656
	s_and_saveexec_b64 s[0:1], vcc
	v_lshl_add_u32 v173, v249, 2, 0
	v_add_u32_e32 v173, 0x27c00, v173
	ds_write_b32 v173, v172
	s_or_b64 exec, exec, s[0:1]
	v_lshrrev_b32_e32 v176, 16, v22
	v_lshlrev_b32_e32 v22, 16, v23
	v_or_b32_sdwa v172, v22, v21 dst_sel:DWORD dst_unused:UNUSED_PAD src0_sel:DWORD src1_sel:WORD_0
	v_lshlrev_b32_e32 v21, 16, v28
	v_or_b32_sdwa v173, v21, v25 dst_sel:DWORD dst_unused:UNUSED_PAD src0_sel:DWORD src1_sel:WORD_0
	v_lshlrev_b32_e32 v21, 16, v33
	v_lshlrev_b32_e32 v19, 16, v19
	v_lshrrev_b32_e32 v177, 16, v174
	v_or_b32_sdwa v174, v21, v31 dst_sel:DWORD dst_unused:UNUSED_PAD src0_sel:DWORD src1_sel:WORD_0
	v_lshlrev_b32_e32 v21, 16, v171
	v_or_b32_sdwa v20, v19, v20 dst_sel:DWORD dst_unused:UNUSED_PAD src0_sel:DWORD src1_sel:WORD_0
	v_lshlrev_b32_e32 v19, 16, v27
	v_or_b32_sdwa v175, v21, v168 dst_sel:DWORD dst_unused:UNUSED_PAD src0_sel:DWORD src1_sel:WORD_0
	v_or_b32_sdwa v21, v19, v24 dst_sel:DWORD dst_unused:UNUSED_PAD src0_sel:DWORD src1_sel:WORD_0
	v_lshlrev_b32_e32 v19, 16, v32
	s_mov_b32 s0, 0xffff0000
	v_lshrrev_b32_e32 v30, 16, v30
	v_lshrrev_b32_e32 v178, 16, v178
	v_or_b32_sdwa v22, v19, v29 dst_sel:DWORD dst_unused:UNUSED_PAD src0_sel:DWORD src1_sel:WORD_0
	v_lshlrev_b32_e32 v19, 16, v169
	v_and_or_b32 v24, v18, s0, v176
	v_mul_u32_u24_e32 v18, 0x48, v249
	v_or_b32_sdwa v23, v19, v167 dst_sel:DWORD dst_unused:UNUSED_PAD src0_sel:DWORD src1_sel:WORD_0
	v_and_or_b32 v25, v26, s0, v30
	v_and_or_b32 v26, v166, s0, v177
	v_and_or_b32 v27, v170, s0, v178
	v_lshlrev_b32_e32 v18, 1, v18
	v_lshlrev_b32_e32 v19, 4, v248
	s_movk_i32 s0, 0x480
	v_add3_u32 v18, 0, v18, v19
	v_cmp_gt_i32_e32 vcc, s0, v0
	ds_write_b128 v18, v[172:175] offset:36864
	ds_write_b128 v18, v[20:23] offset:46080
	ds_write_b128 v18, v[24:27] offset:55296
	s_and_saveexec_b64 s[0:1], vcc
	s_cbranch_execz .LBB0_612
	v_add_u32_e32 v18, 0xfffffe00, v0
	v_lshl_add_u32 v0, v0, 4, s96
	s_mov_b64 s[2:3], 0
